# gdn_scan chain: next chunk's u0/decay loads issued before the qk*v_new MFMA batch (vector-memory issue overlaps MFMAs), on top of v87
# speedup vs baseline: 1.0066x; 1.0022x over previous
.LBB0_490:
	s_bitcmp1_b32 s35, 0
	s_cselect_b32 s26, 0xea00, 0
	v_add_u32_e32 v159, s26, v157
	v_add_u32_e32 v190, v159, v155
	ds_read2_b64 v[68:71], v190 offset1:2
	ds_read2_b64 v[84:87], v190 offset0:4 offset1:6
	ds_read2_b64 v[88:91], v190 offset0:8 offset1:10
	ds_read2_b64 v[92:95], v190 offset0:12 offset1:14
	ds_read2_b64 v[96:99], v190 offset0:16 offset1:18
	ds_read2_b64 v[100:103], v190 offset0:20 offset1:22
	ds_read2_b64 v[104:107], v190 offset0:24 offset1:26
	ds_read2_b64 v[108:111], v190 offset0:28 offset1:30
	v_add_u32_e32 v112, 0x2000, v190
	v_add_u32_e32 v182, 0x2000, v190
	v_add_u32_e32 v186, 0x2000, v190
	v_add_u32_e32 v214, 0x2000, v190
	ds_read2_b64 v[112:115], v112 offset0:48 offset1:50
	ds_read2_b64 v[182:185], v182 offset0:52 offset1:54
	ds_read2_b64 v[186:189], v186 offset0:56 offset1:58
	ds_read2_b64 v[214:217], v214 offset0:60 offset1:62
	v_cvt_pk_bf16_f32 v116, v52, v53
	v_cvt_pk_bf16_f32 v117, v54, v55
	v_cvt_pk_bf16_f32 v118, v56, v57
	v_cvt_pk_bf16_f32 v119, v58, v59
	v_cvt_pk_bf16_f32 v120, v60, v61
	v_cvt_pk_bf16_f32 v121, v62, v63
	v_cvt_pk_bf16_f32 v122, v64, v65
	v_cvt_pk_bf16_f32 v123, v66, v67
	v_cvt_pk_bf16_f32 v124, v36, v37
	v_cvt_pk_bf16_f32 v125, v38, v39
	v_cvt_pk_bf16_f32 v126, v40, v41
	v_cvt_pk_bf16_f32 v127, v42, v43
	v_cvt_pk_bf16_f32 v128, v44, v45
	v_cvt_pk_bf16_f32 v129, v46, v47
	v_cvt_pk_bf16_f32 v130, v48, v49
	v_cvt_pk_bf16_f32 v131, v50, v51
	v_cvt_pk_bf16_f32 v132, v20, v21
	v_cvt_pk_bf16_f32 v133, v22, v23
	v_cvt_pk_bf16_f32 v134, v24, v25
	v_cvt_pk_bf16_f32 v135, v26, v27
	v_cvt_pk_bf16_f32 v136, v28, v29
	v_cvt_pk_bf16_f32 v137, v30, v31
	v_cvt_pk_bf16_f32 v138, v32, v33
	v_cvt_pk_bf16_f32 v139, v34, v35
	v_cvt_pk_bf16_f32 v140, v4, v5
	v_cvt_pk_bf16_f32 v141, v6, v7
	v_cvt_pk_bf16_f32 v142, v8, v9
	v_cvt_pk_bf16_f32 v143, v10, v11
	v_cvt_pk_bf16_f32 v144, v12, v13
	v_cvt_pk_bf16_f32 v145, v14, v15
	v_cvt_pk_bf16_f32 v146, v16, v17
	v_cvt_pk_bf16_f32 v147, v18, v19
	s_waitcnt lgkmcnt(4)
	v_mfma_f32_32x32x16_bf16 v[68:83], v[68:71], v[116:119], 0
	v_mfma_f32_32x32x16_bf16 v[68:83], v[84:87], v[120:123], v[68:83]
	v_add_u32_e32 v84, 0x2000, v190
	ds_read2_b64 v[84:87], v84 offset0:32 offset1:34
	v_mfma_f32_32x32x16_bf16 v[68:83], v[88:91], v[124:127], v[68:83]
	v_mfma_f32_32x32x16_bf16 v[68:83], v[92:95], v[128:131], v[68:83]
	v_mfma_f32_32x32x16_bf16 v[68:83], v[96:99], v[132:135], v[68:83]
	v_mfma_f32_32x32x16_bf16 v[68:83], v[100:103], v[136:139], v[68:83]
	v_add_u32_e32 v100, 0x2000, v190
	ds_read2_b64 v[100:103], v100 offset0:36 offset1:38
	v_mfma_f32_32x32x16_bf16 v[68:83], v[104:107], v[140:143], v[68:83]
	v_add_u32_e32 v104, 0x2000, v190
	ds_read2_b64 v[104:107], v104 offset0:40 offset1:42
	v_mfma_f32_32x32x16_bf16 v[68:83], v[108:111], v[144:147], v[68:83]
	v_add_u32_e32 v108, 0x2000, v190
	ds_read2_b64 v[108:111], v108 offset0:44 offset1:46
	v_add_u32_e32 v88, 0x2000, v190
	s_waitcnt lgkmcnt(3)
	v_mfma_f32_32x32x16_bf16 v[84:99], v[84:87], v[116:119], 0
	s_waitcnt lgkmcnt(2)
	v_mfma_f32_32x32x16_bf16 v[84:99], v[100:103], v[120:123], v[84:99]
	s_waitcnt lgkmcnt(1)
	v_mfma_f32_32x32x16_bf16 v[84:99], v[104:107], v[124:127], v[84:99]
	s_waitcnt lgkmcnt(0)
	v_mfma_f32_32x32x16_bf16 v[84:99], v[108:111], v[128:131], v[84:99]
	v_mfma_f32_32x32x16_bf16 v[84:99], v[112:115], v[132:135], v[84:99]
	v_mfma_f32_32x32x16_bf16 v[84:99], v[182:185], v[136:139], v[84:99]
	v_mfma_f32_32x32x16_bf16 v[84:99], v[186:189], v[140:143], v[84:99]
	v_mfma_f32_32x32x16_bf16 v[84:99], v[214:217], v[144:147], v[84:99]
	s_waitcnt vmcnt(32)
	v_mov_b32_e32 v200, v201
	v_sub_f32_e32 v81, v197, v81
	v_sub_f32_e32 v80, v196, v80
	v_sub_f32_e32 v71, v165, v71
	v_sub_f32_e32 v70, v164, v70
	v_sub_f32_e32 v69, v167, v69
	v_sub_f32_e32 v68, v166, v68
	v_cvt_pk_bf16_f32 v106, v80, v81
	s_nop 3
	v_sub_f32_e32 v80, v175, v87
	v_sub_f32_e32 v81, v174, v86
	v_sub_f32_e32 v83, v199, v83
	v_sub_f32_e32 v82, v198, v82
	v_sub_f32_e32 v79, v195, v79
	v_sub_f32_e32 v78, v194, v78
	v_sub_f32_e32 v77, v181, v77
	v_sub_f32_e32 v76, v180, v76
	v_sub_f32_e32 v75, v171, v75
	v_sub_f32_e32 v74, v170, v74
	v_sub_f32_e32 v73, v169, v73
	v_sub_f32_e32 v72, v168, v72
	v_cvt_pk_bf16_f32 v100, v68, v69
	v_cvt_pk_bf16_f32 v101, v70, v71
	v_sub_f32_e32 v68, v179, v91
	v_sub_f32_e32 v69, v178, v90
	v_sub_f32_e32 v70, v177, v89
	v_sub_f32_e32 v71, v176, v88
	v_cvt_pk_bf16_f32 v109, v81, v80
	v_add_u32_e32 v80, 0x4000, v190
	v_cvt_pk_bf16_f32 v102, v72, v73
	v_cvt_pk_bf16_f32 v103, v74, v75
	v_cvt_pk_bf16_f32 v104, v76, v77
	v_cvt_pk_bf16_f32 v105, v78, v79
	v_cvt_pk_bf16_f32 v107, v82, v83
	v_sub_f32_e32 v72, v209, v99
	v_sub_f32_e32 v73, v208, v98
	v_sub_f32_e32 v74, v207, v97
	v_sub_f32_e32 v75, v206, v96
	v_sub_f32_e32 v76, v205, v95
	v_sub_f32_e32 v77, v204, v94
	v_sub_f32_e32 v78, v203, v93
	v_sub_f32_e32 v79, v202, v92
	v_sub_f32_e32 v82, v173, v85
	v_sub_f32_e32 v83, v172, v84
	v_cvt_pk_bf16_f32 v110, v71, v70
	v_cvt_pk_bf16_f32 v111, v69, v68
	ds_read2_b64 v[68:71], v80 offset0:64 offset1:66
	ds_read2_b64 v[84:87], v80 offset0:68 offset1:70
	ds_read2_b64 v[88:91], v80 offset0:72 offset1:74
	ds_read2_b64 v[92:95], v80 offset0:76 offset1:78
	ds_read2_b64 v[96:99], v80 offset0:80 offset1:82
	ds_read2_b64 v[164:167], v80 offset0:84 offset1:86
	ds_read2_b64 v[168:171], v80 offset0:88 offset1:90
	ds_read2_b64 v[172:175], v80 offset0:92 offset1:94
	v_add_u32_e32 v176, 0x6000, v190
	v_add_u32_e32 v180, 0x6000, v190
	v_add_u32_e32 v184, 0x6000, v190
	v_add_u32_e32 v194, 0x6000, v190
	ds_read2_b64 v[176:179], v176 offset0:112 offset1:114
	ds_read2_b64 v[180:183], v180 offset0:116 offset1:118
	ds_read2_b64 v[184:187], v184 offset0:120 offset1:122
	ds_read2_b64 v[194:197], v194 offset0:124 offset1:126
	v_cvt_pk_bf16_f32 v108, v83, v82
	v_cvt_pk_bf16_f32 v112, v79, v78
	v_cvt_pk_bf16_f32 v113, v77, v76
	v_cvt_pk_bf16_f32 v114, v75, v74
	v_cvt_pk_bf16_f32 v115, v73, v72
	s_waitcnt lgkmcnt(11)
	v_mfma_f32_32x32x16_bf16 v[68:83], v[68:71], v[116:119], 0
	s_waitcnt lgkmcnt(10)
	v_mfma_f32_32x32x16_bf16 v[68:83], v[84:87], v[120:123], v[68:83]
	v_add_u32_e32 v84, 0x6000, v190
	ds_read2_b64 v[84:87], v84 offset0:96 offset1:98
	s_waitcnt lgkmcnt(10)
	v_mfma_f32_32x32x16_bf16 v[68:83], v[88:91], v[124:127], v[68:83]
	s_waitcnt lgkmcnt(9)
	v_mfma_f32_32x32x16_bf16 v[68:83], v[92:95], v[128:131], v[68:83]
	s_waitcnt lgkmcnt(8)
	v_mfma_f32_32x32x16_bf16 v[68:83], v[96:99], v[132:135], v[68:83]
	s_waitcnt lgkmcnt(7)
	v_mfma_f32_32x32x16_bf16 v[68:83], v[164:167], v[136:139], v[68:83]
	v_add_u32_e32 v164, 0x6000, v190
	ds_read2_b64 v[164:167], v164 offset0:100 offset1:102
	s_waitcnt lgkmcnt(7)
	v_mfma_f32_32x32x16_bf16 v[68:83], v[168:171], v[140:143], v[68:83]
	v_add_u32_e32 v168, 0x6000, v190
	ds_read2_b64 v[168:171], v168 offset0:104 offset1:106
	s_waitcnt lgkmcnt(7)
	v_mfma_f32_32x32x16_bf16 v[68:83], v[172:175], v[144:147], v[68:83]
	v_add_u32_e32 v172, 0x6000, v190
	ds_read2_b64 v[172:175], v172 offset0:108 offset1:110
	v_add_u32_e32 v88, 0x6000, v190
	s_waitcnt lgkmcnt(3)
	v_mfma_f32_32x32x16_bf16 v[84:99], v[84:87], v[116:119], 0
	v_add_u32_e32 v116, v159, v153
	v_add_u32_e32 v116, 0x8000, v116
	ds_read2_b64 v[116:119], v116 offset0:128 offset1:130
	s_waitcnt lgkmcnt(3)
	v_mfma_f32_32x32x16_bf16 v[84:99], v[164:167], v[120:123], v[84:99]
	v_add_u32_e32 v120, v159, v153
	v_add_u32_e32 v120, 0x8000, v120
	ds_read2_b64 v[120:123], v120 offset0:132 offset1:134
	s_waitcnt lgkmcnt(3)
	v_mfma_f32_32x32x16_bf16 v[84:99], v[168:171], v[124:127], v[84:99]
	v_add_u32_e32 v124, v159, v153
	v_add_u32_e32 v124, 0x8000, v124
	ds_read2_b64 v[124:127], v124 offset0:136 offset1:138
	s_waitcnt lgkmcnt(3)
	v_mfma_f32_32x32x16_bf16 v[84:99], v[172:175], v[128:131], v[84:99]
	v_add_u32_e32 v128, v159, v153
	v_add_u32_e32 v128, 0x8000, v128
	ds_read2_b64 v[128:131], v128 offset0:140 offset1:142
	v_mfma_f32_32x32x16_bf16 v[84:99], v[176:179], v[132:135], v[84:99]
	v_add_u32_e32 v132, v159, v153
	v_add_u32_e32 v132, 0x9000, v132
	ds_read2_b64 v[132:135], v132 offset0:160 offset1:162
	v_mfma_f32_32x32x16_bf16 v[84:99], v[180:183], v[136:139], v[84:99]
	v_add_u32_e32 v136, v159, v153
	v_add_u32_e32 v136, 0x9000, v136
	ds_read2_b64 v[136:139], v136 offset0:164 offset1:166
	v_mfma_f32_32x32x16_bf16 v[84:99], v[184:187], v[140:143], v[84:99]
	v_add_u32_e32 v140, v159, v153
	v_add_u32_e32 v140, 0x9000, v140
	ds_read2_b64 v[140:143], v140 offset0:168 offset1:170
	v_mfma_f32_32x32x16_bf16 v[84:99], v[194:197], v[144:147], v[84:99]
	v_add_u32_e32 v144, v159, v153
	v_add_u32_e32 v144, 0x9000, v144
	ds_read2_b64 v[144:147], v144 offset0:172 offset1:174
	v_add_u32_e32 v159, v159, v153
	v_lshl_add_u64 v[182:183], s[6:7], 0, v[162:163]
	s_mov_b32 s26, 0x41a20000
	v_add_co_u32_e32 v218, vcc, s26, v182
	s_nop 1
	v_addc_co_u32_e32 v219, vcc, 0, v183, vcc
	s_mov_b32 s26, 0x41a21000
	v_add_co_u32_e32 v220, vcc, s26, v182
	s_nop 1
	v_addc_co_u32_e32 v221, vcc, 0, v183, vcc
	s_mov_b32 s26, 0x41a24000
	v_add_co_u32_e32 v222, vcc, s26, v182
	s_nop 1
	v_addc_co_u32_e32 v223, vcc, 0, v183, vcc
	s_mov_b32 s26, 0x41a25000
	v_add_co_u32_e32 v224, vcc, s26, v182
	s_nop 1
	v_addc_co_u32_e32 v225, vcc, 0, v183, vcc
	global_load_dword v166, v[218:219], off
	global_load_dword v167, v[218:219], off offset:2048
	global_load_dword v164, v[220:221], off
	global_load_dword v165, v[220:221], off offset:2048
	global_load_dword v168, v[222:223], off
	global_load_dword v169, v[222:223], off offset:2048
	global_load_dword v170, v[224:225], off
	global_load_dword v171, v[224:225], off offset:2048
	s_mov_b32 s26, 0x41a28000
	v_add_co_u32_e32 v218, vcc, s26, v182
	s_nop 1
	v_addc_co_u32_e32 v219, vcc, 0, v183, vcc
	s_mov_b32 s26, 0x41a29000
	v_add_co_u32_e32 v220, vcc, s26, v182
	s_nop 1
	v_addc_co_u32_e32 v221, vcc, 0, v183, vcc
	s_mov_b32 s26, 0x41a2c000
	v_add_co_u32_e32 v222, vcc, s26, v182
	s_nop 1
	v_addc_co_u32_e32 v223, vcc, 0, v183, vcc
	s_mov_b32 s26, 0x41a2d000
	v_add_co_u32_e32 v224, vcc, s26, v182
	s_nop 1
	v_addc_co_u32_e32 v225, vcc, 0, v183, vcc
	global_load_dword v180, v[218:219], off
	global_load_dword v181, v[218:219], off offset:2048
	global_load_dword v194, v[220:221], off
	global_load_dword v195, v[220:221], off offset:2048
	global_load_dword v196, v[222:223], off
	global_load_dword v197, v[222:223], off offset:2048
	global_load_dword v198, v[224:225], off
	global_load_dword v199, v[224:225], off offset:2048
	s_mov_b32 s26, 0x41a30000
	v_add_co_u32_e32 v218, vcc, s26, v182
	s_nop 1
	v_addc_co_u32_e32 v219, vcc, 0, v183, vcc
	s_mov_b32 s26, 0x41a31000
	v_add_co_u32_e32 v220, vcc, s26, v182
	s_nop 1
	v_addc_co_u32_e32 v221, vcc, 0, v183, vcc
	s_mov_b32 s26, 0x41a34000
	v_add_co_u32_e32 v222, vcc, s26, v182
	s_nop 1
	v_addc_co_u32_e32 v223, vcc, 0, v183, vcc
	s_mov_b32 s26, 0x41a35000
	v_add_co_u32_e32 v224, vcc, s26, v182
	s_nop 1
	v_addc_co_u32_e32 v225, vcc, 0, v183, vcc
	global_load_dword v172, v[218:219], off
	global_load_dword v173, v[218:219], off offset:2048
	global_load_dword v174, v[220:221], off
	global_load_dword v175, v[220:221], off offset:2048
	global_load_dword v176, v[222:223], off
	global_load_dword v177, v[222:223], off offset:2048
	global_load_dword v178, v[224:225], off
	global_load_dword v179, v[224:225], off offset:2048
	s_mov_b32 s26, 0x41a38000
	v_add_co_u32_e32 v218, vcc, s26, v182
	s_nop 1
	v_addc_co_u32_e32 v219, vcc, 0, v183, vcc
	s_mov_b32 s26, 0x41a39000
	v_add_co_u32_e32 v220, vcc, s26, v182
	s_nop 1
	v_addc_co_u32_e32 v221, vcc, 0, v183, vcc
	s_mov_b32 s26, 0x41a3c000
	v_add_co_u32_e32 v222, vcc, s26, v182
	s_nop 1
	v_addc_co_u32_e32 v223, vcc, 0, v183, vcc
	s_mov_b32 s26, 0x41a3d000
	v_add_co_u32_e32 v224, vcc, s26, v182
	s_nop 1
	v_addc_co_u32_e32 v225, vcc, 0, v183, vcc
	global_load_dword v202, v[218:219], off
	global_load_dword v203, v[218:219], off offset:2048
	global_load_dword v204, v[220:221], off
	global_load_dword v205, v[220:221], off offset:2048
	global_load_dword v206, v[222:223], off
	global_load_dword v207, v[222:223], off offset:2048
	global_load_dword v208, v[224:225], off
	global_load_dword v209, v[224:225], off offset:2048
	s_add_i32 s35, s35, 1
	s_add_u32 s26, s6, s28
	s_addc_u32 s27, s7, s29
	v_mov_b64_e32 v[232:233], s[26:27]
	global_load_dword v201, v[232:233], off
	s_waitcnt lgkmcnt(7)
	v_mfma_f32_32x32x16_bf16 v[68:83], v[116:119], v[100:103], v[68:83]
	s_waitcnt lgkmcnt(3)
	v_mfma_f32_32x32x16_bf16 v[84:99], v[132:135], v[100:103], v[84:99]
	v_mfma_f32_32x32x16_bf16 v[68:83], v[120:123], v[104:107], v[68:83]
	s_waitcnt lgkmcnt(2)
	v_mfma_f32_32x32x16_bf16 v[84:99], v[136:139], v[104:107], v[84:99]
	v_mfma_f32_32x32x16_bf16 v[68:83], v[124:127], v[108:111], v[68:83]
	s_waitcnt lgkmcnt(1)
	v_mfma_f32_32x32x16_bf16 v[84:99], v[140:143], v[108:111], v[84:99]
	v_mfma_f32_32x32x16_bf16 v[68:83], v[128:131], v[112:115], v[68:83]
	s_waitcnt lgkmcnt(0)
	v_mfma_f32_32x32x16_bf16 v[84:99], v[144:147], v[112:115], v[84:99]
	v_lshl_add_u64 v[116:117], s[6:7], 0, v[162:163]
	s_mov_b32 s26, 0x47200000
	v_add_co_u32_e32 v218, vcc, s26, v116
	s_nop 1
	v_addc_co_u32_e32 v219, vcc, 0, v117, vcc
	s_mov_b32 s26, 0x47201000
	v_add_co_u32_e32 v220, vcc, s26, v116
	s_nop 1
	v_addc_co_u32_e32 v221, vcc, 0, v117, vcc
	s_mov_b32 s26, 0x47204000
	v_add_co_u32_e32 v222, vcc, s26, v116
	s_nop 1
	v_addc_co_u32_e32 v223, vcc, 0, v117, vcc
	s_mov_b32 s26, 0x47205000
	v_add_co_u32_e32 v224, vcc, s26, v116
	s_nop 1
	v_addc_co_u32_e32 v225, vcc, 0, v117, vcc
	global_store_dword v[218:219], v68, off
	global_store_dword v[218:219], v69, off offset:2048
	global_store_dword v[220:221], v70, off
	global_store_dword v[220:221], v71, off offset:2048
	global_store_dword v[222:223], v72, off
	global_store_dword v[222:223], v73, off offset:2048
	global_store_dword v[224:225], v74, off
	global_store_dword v[224:225], v75, off offset:2048
	s_mov_b32 s26, 0x47208000
	v_add_co_u32_e32 v218, vcc, s26, v116
	s_nop 1
	v_addc_co_u32_e32 v219, vcc, 0, v117, vcc
	s_mov_b32 s26, 0x47209000
	v_add_co_u32_e32 v220, vcc, s26, v116
	s_nop 1
	v_addc_co_u32_e32 v221, vcc, 0, v117, vcc
	s_mov_b32 s26, 0x4720c000
	v_add_co_u32_e32 v222, vcc, s26, v116
	s_nop 1
	v_addc_co_u32_e32 v223, vcc, 0, v117, vcc
	s_mov_b32 s26, 0x4720d000
	v_add_co_u32_e32 v224, vcc, s26, v116
	s_nop 1
	v_addc_co_u32_e32 v225, vcc, 0, v117, vcc
	global_store_dword v[218:219], v76, off
	global_store_dword v[218:219], v77, off offset:2048
	global_store_dword v[220:221], v78, off
	global_store_dword v[220:221], v79, off offset:2048
	global_store_dword v[222:223], v80, off
	global_store_dword v[222:223], v81, off offset:2048
	global_store_dword v[224:225], v82, off
	global_store_dword v[224:225], v83, off offset:2048
	s_mov_b32 s26, 0x47210000
	v_add_co_u32_e32 v218, vcc, s26, v116
	s_nop 1
	v_addc_co_u32_e32 v219, vcc, 0, v117, vcc
	s_mov_b32 s26, 0x47211000
	v_add_co_u32_e32 v220, vcc, s26, v116
	s_nop 1
	v_addc_co_u32_e32 v221, vcc, 0, v117, vcc
	s_mov_b32 s26, 0x47214000
	v_add_co_u32_e32 v222, vcc, s26, v116
	s_nop 1
	v_addc_co_u32_e32 v223, vcc, 0, v117, vcc
	s_mov_b32 s26, 0x47215000
	v_add_co_u32_e32 v224, vcc, s26, v116
	s_nop 1
	v_addc_co_u32_e32 v225, vcc, 0, v117, vcc
	global_store_dword v[218:219], v84, off
	global_store_dword v[218:219], v85, off offset:2048
	global_store_dword v[220:221], v86, off
	global_store_dword v[220:221], v87, off offset:2048
	global_store_dword v[222:223], v88, off
	global_store_dword v[222:223], v89, off offset:2048
	global_store_dword v[224:225], v90, off
	global_store_dword v[224:225], v91, off offset:2048
	s_mov_b32 s26, 0x47218000
	v_add_co_u32_e32 v218, vcc, s26, v116
	s_nop 1
	v_addc_co_u32_e32 v219, vcc, 0, v117, vcc
	s_mov_b32 s26, 0x47219000
	v_add_co_u32_e32 v220, vcc, s26, v116
	s_nop 1
	v_addc_co_u32_e32 v221, vcc, 0, v117, vcc
	s_mov_b32 s26, 0x4721c000
	v_add_co_u32_e32 v222, vcc, s26, v116
	s_nop 1
	v_addc_co_u32_e32 v223, vcc, 0, v117, vcc
	s_mov_b32 s26, 0x4721d000
	v_add_co_u32_e32 v224, vcc, s26, v116
	s_nop 1
	v_addc_co_u32_e32 v225, vcc, 0, v117, vcc
	global_store_dword v[218:219], v92, off
	global_store_dword v[218:219], v93, off offset:2048
	global_store_dword v[220:221], v94, off
	global_store_dword v[220:221], v95, off offset:2048
	global_store_dword v[222:223], v96, off
	global_store_dword v[222:223], v97, off offset:2048
	global_store_dword v[224:225], v98, off
	global_store_dword v[224:225], v99, off offset:2048
	v_add_u32_e32 v80, 0xa000, v159
	v_add_u32_e32 v96, 0xb000, v159
	ds_read2_b64 v[68:71], v80 offset0:192 offset1:194
	ds_read2_b64 v[72:75], v80 offset0:196 offset1:198
	ds_read2_b64 v[76:79], v80 offset0:200 offset1:202
	ds_read2_b64 v[80:83], v80 offset0:204 offset1:206
	ds_read2_b64 v[84:87], v96 offset0:224 offset1:226
	ds_read2_b64 v[88:91], v96 offset0:228 offset1:230
	ds_read2_b64 v[92:95], v96 offset0:232 offset1:234
	ds_read2_b64 v[96:99], v96 offset0:236 offset1:238
	v_pk_mul_f32 v[66:67], v[66:67], v[200:201] op_sel_hi:[1,0]
	v_pk_mul_f32 v[64:65], v[64:65], v[200:201] op_sel_hi:[1,0]
	v_pk_mul_f32 v[62:63], v[62:63], v[200:201] op_sel_hi:[1,0]
	v_pk_mul_f32 v[60:61], v[60:61], v[200:201] op_sel_hi:[1,0]
	v_pk_mul_f32 v[58:59], v[58:59], v[200:201] op_sel_hi:[1,0]
	v_pk_mul_f32 v[56:57], v[56:57], v[200:201] op_sel_hi:[1,0]
	v_pk_mul_f32 v[54:55], v[54:55], v[200:201] op_sel_hi:[1,0]
	v_pk_mul_f32 v[52:53], v[52:53], v[200:201] op_sel_hi:[1,0]
	v_pk_mul_f32 v[50:51], v[50:51], v[200:201] op_sel_hi:[1,0]
	v_pk_mul_f32 v[48:49], v[48:49], v[200:201] op_sel_hi:[1,0]
	v_pk_mul_f32 v[46:47], v[46:47], v[200:201] op_sel_hi:[1,0]
	v_pk_mul_f32 v[44:45], v[44:45], v[200:201] op_sel_hi:[1,0]
	v_pk_mul_f32 v[42:43], v[42:43], v[200:201] op_sel_hi:[1,0]
	v_pk_mul_f32 v[40:41], v[40:41], v[200:201] op_sel_hi:[1,0]
	v_pk_mul_f32 v[38:39], v[38:39], v[200:201] op_sel_hi:[1,0]
	v_pk_mul_f32 v[36:37], v[36:37], v[200:201] op_sel_hi:[1,0]
	s_waitcnt lgkmcnt(0)
	v_mfma_f32_32x32x16_bf16 v[52:67], v[68:71], v[100:103], v[52:67]
	v_mfma_f32_32x32x16_bf16 v[36:51], v[84:87], v[100:103], v[36:51]
	v_mfma_f32_32x32x16_bf16 v[52:67], v[72:75], v[104:107], v[52:67]
	v_mfma_f32_32x32x16_bf16 v[36:51], v[88:91], v[104:107], v[36:51]
	v_mfma_f32_32x32x16_bf16 v[52:67], v[76:79], v[108:111], v[52:67]
	v_mfma_f32_32x32x16_bf16 v[36:51], v[92:95], v[108:111], v[36:51]
	v_mfma_f32_32x32x16_bf16 v[52:67], v[80:83], v[112:115], v[52:67]
	v_mfma_f32_32x32x16_bf16 v[36:51], v[96:99], v[112:115], v[36:51]
	v_add_u32_e32 v80, 0xc800, v159
	v_add_u32_e32 v96, 0xd800, v159
	ds_read2_b64 v[68:71], v80 offset1:2
	ds_read2_b64 v[72:75], v80 offset0:4 offset1:6
	ds_read2_b64 v[76:79], v80 offset0:8 offset1:10
	ds_read2_b64 v[80:83], v80 offset0:12 offset1:14
	ds_read2_b64 v[84:87], v96 offset0:32 offset1:34
	ds_read2_b64 v[88:91], v96 offset0:36 offset1:38
	ds_read2_b64 v[92:95], v96 offset0:40 offset1:42
	ds_read2_b64 v[96:99], v96 offset0:44 offset1:46
	v_pk_mul_f32 v[34:35], v[34:35], v[200:201] op_sel_hi:[1,0]
	v_pk_mul_f32 v[32:33], v[32:33], v[200:201] op_sel_hi:[1,0]
	v_pk_mul_f32 v[30:31], v[30:31], v[200:201] op_sel_hi:[1,0]
	v_pk_mul_f32 v[28:29], v[28:29], v[200:201] op_sel_hi:[1,0]
	v_pk_mul_f32 v[26:27], v[26:27], v[200:201] op_sel_hi:[1,0]
	v_pk_mul_f32 v[24:25], v[24:25], v[200:201] op_sel_hi:[1,0]
	v_pk_mul_f32 v[22:23], v[22:23], v[200:201] op_sel_hi:[1,0]
	v_pk_mul_f32 v[20:21], v[20:21], v[200:201] op_sel_hi:[1,0]
	v_pk_mul_f32 v[18:19], v[18:19], v[200:201] op_sel_hi:[1,0]
	v_pk_mul_f32 v[16:17], v[16:17], v[200:201] op_sel_hi:[1,0]
	v_pk_mul_f32 v[14:15], v[14:15], v[200:201] op_sel_hi:[1,0]
	v_pk_mul_f32 v[12:13], v[12:13], v[200:201] op_sel_hi:[1,0]
	v_pk_mul_f32 v[10:11], v[10:11], v[200:201] op_sel_hi:[1,0]
	v_pk_mul_f32 v[8:9], v[8:9], v[200:201] op_sel_hi:[1,0]
	v_pk_mul_f32 v[6:7], v[6:7], v[200:201] op_sel_hi:[1,0]
	v_pk_mul_f32 v[4:5], v[4:5], v[200:201] op_sel_hi:[1,0]
	s_waitcnt lgkmcnt(0)
	v_mfma_f32_32x32x16_bf16 v[20:35], v[68:71], v[100:103], v[20:35]
	v_mfma_f32_32x32x16_bf16 v[4:19], v[84:87], v[100:103], v[4:19]
	v_mfma_f32_32x32x16_bf16 v[20:35], v[72:75], v[104:107], v[20:35]
	v_mfma_f32_32x32x16_bf16 v[4:19], v[88:91], v[104:107], v[4:19]
	v_mfma_f32_32x32x16_bf16 v[20:35], v[76:79], v[108:111], v[20:35]
	v_mfma_f32_32x32x16_bf16 v[4:19], v[92:95], v[108:111], v[4:19]
	v_mfma_f32_32x32x16_bf16 v[20:35], v[80:83], v[112:115], v[20:35]
	v_mfma_f32_32x32x16_bf16 v[4:19], v[96:99], v[112:115], v[4:19]
	s_add_u32 s28, s28, 4
	s_addc_u32 s29, s29, 0
	v_lshl_add_u64 v[162:163], v[162:163], 0, s[38:39]
	s_cmp_eq_u32 s35, 63
	s_barrier
	s_cbranch_scc0 .LBB0_490
	s_waitcnt vmcnt(32)
	v_add_u32_e32 v82, v157, v155
	v_cvt_pk_bf16_f32 v52, v52, v53
	v_cvt_pk_bf16_f32 v53, v54, v55
	v_cvt_pk_bf16_f32 v54, v56, v57
	v_cvt_pk_bf16_f32 v57, v62, v63
	v_cvt_pk_bf16_f32 v62, v8, v9
	v_add_u32_e32 v8, 0xe800, v82
	v_cvt_pk_bf16_f32 v56, v60, v61
	v_cvt_pk_bf16_f32 v36, v36, v37
	v_cvt_pk_bf16_f32 v37, v38, v39
	v_cvt_pk_bf16_f32 v38, v40, v41
	v_cvt_pk_bf16_f32 v39, v42, v43
	v_cvt_pk_bf16_f32 v40, v44, v45
	v_cvt_pk_bf16_f32 v41, v46, v47
	v_cvt_pk_bf16_f32 v42, v48, v49
	v_cvt_pk_bf16_f32 v43, v50, v51
	v_cvt_pk_bf16_f32 v44, v20, v21
	v_cvt_pk_bf16_f32 v45, v22, v23
	v_cvt_pk_bf16_f32 v46, v24, v25
	v_cvt_pk_bf16_f32 v47, v26, v27
	v_cvt_pk_bf16_f32 v48, v28, v29
	v_cvt_pk_bf16_f32 v49, v30, v31
	v_cvt_pk_bf16_f32 v50, v32, v33
	v_cvt_pk_bf16_f32 v51, v34, v35
	v_cvt_pk_bf16_f32 v60, v4, v5
	v_cvt_pk_bf16_f32 v61, v6, v7
	ds_read2_b64 v[4:7], v8 offset0:64 offset1:66
	ds_read2_b64 v[20:23], v8 offset0:68 offset1:70
	ds_read2_b64 v[24:27], v8 offset0:72 offset1:74
	ds_read2_b64 v[28:31], v8 offset0:76 offset1:78
	ds_read2_b64 v[32:35], v8 offset0:80 offset1:82
	ds_read2_b64 v[68:71], v8 offset0:84 offset1:86
	ds_read2_b64 v[72:75], v8 offset0:88 offset1:90
	ds_read2_b64 v[78:81], v8 offset0:92 offset1:94
	s_add_u32 s24, s6, s24
	s_addc_u32 s25, s7, s25
	s_add_u32 s24, s24, s9
	s_addc_u32 s25, s25, 0
	v_lshl_add_u64 v[76:77], v[160:161], 2, s[24:25]
	v_cvt_pk_bf16_f32 v55, v58, v59
	v_cvt_pk_bf16_f32 v58, v64, v65
	v_cvt_pk_bf16_f32 v59, v66, v67
	v_cvt_pk_bf16_f32 v63, v10, v11
	v_cvt_pk_bf16_f32 v64, v12, v13
	v_cvt_pk_bf16_f32 v65, v14, v15
	v_cvt_pk_bf16_f32 v66, v16, v17
	v_cvt_pk_bf16_f32 v67, v18, v19
	s_waitcnt lgkmcnt(7)
	v_mfma_f32_32x32x16_bf16 v[4:19], v[4:7], v[52:55], 0
	s_waitcnt lgkmcnt(6)
	v_mfma_f32_32x32x16_bf16 v[4:19], v[20:23], v[56:59], v[4:19]
	s_waitcnt lgkmcnt(5)
	v_mfma_f32_32x32x16_bf16 v[4:19], v[24:27], v[36:39], v[4:19]
	s_waitcnt lgkmcnt(4)
	v_mfma_f32_32x32x16_bf16 v[4:19], v[28:31], v[40:43], v[4:19]
	s_waitcnt lgkmcnt(3)
	v_mfma_f32_32x32x16_bf16 v[4:19], v[32:35], v[44:47], v[4:19]
	s_waitcnt lgkmcnt(2)
	v_mfma_f32_32x32x16_bf16 v[4:19], v[68:71], v[48:51], v[4:19]
	s_waitcnt lgkmcnt(1)
	v_mfma_f32_32x32x16_bf16 v[4:19], v[72:75], v[60:63], v[4:19]
	s_waitcnt lgkmcnt(0)
	v_mfma_f32_32x32x16_bf16 v[4:19], v[78:81], v[64:67], v[4:19]
	v_add_u32_e32 v20, 0x2100, v82
	v_add_u32_e32 v24, 0xe800, v20
	ds_read2_b64 v[20:23], v24 offset0:64 offset1:66
	ds_read2_b64 v[68:71], v24 offset0:68 offset1:70
	ds_read2_b64 v[72:75], v24 offset0:72 offset1:74
	ds_read2_b64 v[78:81], v24 offset0:76 offset1:78
	ds_read2_b64 v[82:85], v24 offset0:80 offset1:82
	ds_read2_b64 v[86:89], v24 offset0:84 offset1:86
	ds_read2_b64 v[90:93], v24 offset0:88 offset1:90
	ds_read2_b64 v[94:97], v24 offset0:92 offset1:94
	s_waitcnt lgkmcnt(7)
	v_mfma_f32_32x32x16_bf16 v[20:35], v[20:23], v[52:55], 0
	s_waitcnt lgkmcnt(6)
	v_mfma_f32_32x32x16_bf16 v[20:35], v[68:71], v[56:59], v[20:35]
	s_waitcnt lgkmcnt(5)
	v_mfma_f32_32x32x16_bf16 v[20:35], v[72:75], v[36:39], v[20:35]
	s_waitcnt lgkmcnt(4)
	v_mfma_f32_32x32x16_bf16 v[20:35], v[78:81], v[40:43], v[20:35]
	s_waitcnt lgkmcnt(3)
	v_mfma_f32_32x32x16_bf16 v[20:35], v[82:85], v[44:47], v[20:35]
	s_waitcnt lgkmcnt(2)
	v_mfma_f32_32x32x16_bf16 v[20:35], v[86:89], v[48:51], v[20:35]
	s_waitcnt lgkmcnt(1)
	v_mfma_f32_32x32x16_bf16 v[20:35], v[90:93], v[60:63], v[20:35]
	s_waitcnt lgkmcnt(0)
	v_mfma_f32_32x32x16_bf16 v[20:35], v[94:97], v[64:67], v[20:35]
	v_add_f32_e64 v4, v166, -v4
	v_add_f32_e64 v5, v167, -v5
	v_add_f32_e64 v6, v164, -v6
	v_add_f32_e64 v7, v165, -v7
	v_add_f32_e64 v8, v168, -v8
	v_add_f32_e64 v9, v169, -v9
	v_pk_add_f32 v[10:11], v[170:171], v[10:11] neg_lo:[0,1] neg_hi:[0,1]
	v_pk_add_f32 v[12:13], v[180:181], v[12:13] neg_lo:[0,1] neg_hi:[0,1]
	v_pk_add_f32 v[14:15], v[194:195], v[14:15] neg_lo:[0,1] neg_hi:[0,1]
	v_pk_add_f32 v[16:17], v[196:197], v[16:17] neg_lo:[0,1] neg_hi:[0,1]
	v_pk_add_f32 v[18:19], v[198:199], v[18:19] neg_lo:[0,1] neg_hi:[0,1]
	v_cvt_pk_bf16_f32 v68, v4, v5
	v_cvt_pk_bf16_f32 v69, v6, v7
	v_pk_add_f32 v[4:5], v[172:173], v[20:21] neg_lo:[0,1] neg_hi:[0,1]
	v_pk_add_f32 v[6:7], v[174:175], v[22:23] neg_lo:[0,1] neg_hi:[0,1]
	v_add3_u32 v98, s31, v149, v155
	v_cvt_pk_bf16_f32 v70, v8, v9
	v_cvt_pk_bf16_f32 v71, v10, v11
	v_cvt_pk_bf16_f32 v72, v12, v13
	v_cvt_pk_bf16_f32 v73, v14, v15
	v_cvt_pk_bf16_f32 v74, v16, v17
	v_cvt_pk_bf16_f32 v75, v18, v19
	v_pk_add_f32 v[8:9], v[176:177], v[24:25] neg_lo:[0,1] neg_hi:[0,1]
	v_pk_add_f32 v[10:11], v[178:179], v[26:27] neg_lo:[0,1] neg_hi:[0,1]
	v_pk_add_f32 v[12:13], v[202:203], v[28:29] neg_lo:[0,1] neg_hi:[0,1]
	v_pk_add_f32 v[14:15], v[204:205], v[30:31] neg_lo:[0,1] neg_hi:[0,1]
	v_pk_add_f32 v[16:17], v[206:207], v[32:33] neg_lo:[0,1] neg_hi:[0,1]
	v_pk_add_f32 v[18:19], v[208:209], v[34:35] neg_lo:[0,1] neg_hi:[0,1]
	v_cvt_pk_bf16_f32 v78, v4, v5
	v_cvt_pk_bf16_f32 v79, v6, v7
	ds_read2_b64 v[4:7], v98 offset1:2
	ds_read2_b64 v[20:23], v98 offset0:4 offset1:6
	ds_read2_b64 v[24:27], v98 offset0:8 offset1:10
	ds_read2_b64 v[28:31], v98 offset0:12 offset1:14
	ds_read2_b64 v[32:35], v98 offset0:16 offset1:18
	ds_read2_b64 v[82:85], v98 offset0:20 offset1:22
	ds_read2_b64 v[86:89], v98 offset0:24 offset1:26
	ds_read2_b64 v[90:93], v98 offset0:28 offset1:30
	v_cvt_pk_bf16_f32 v80, v8, v9
	v_cvt_pk_bf16_f32 v81, v10, v11
	v_cvt_pk_bf16_f32 v94, v12, v13
	v_cvt_pk_bf16_f32 v95, v14, v15
	v_cvt_pk_bf16_f32 v96, v16, v17
	v_cvt_pk_bf16_f32 v97, v18, v19
	s_waitcnt lgkmcnt(7)
	v_mfma_f32_32x32x16_bf16 v[4:19], v[4:7], v[52:55], 0
	s_waitcnt lgkmcnt(6)
	v_mfma_f32_32x32x16_bf16 v[4:19], v[20:23], v[56:59], v[4:19]
	s_waitcnt lgkmcnt(5)
	v_mfma_f32_32x32x16_bf16 v[4:19], v[24:27], v[36:39], v[4:19]
	s_waitcnt lgkmcnt(4)
	v_mfma_f32_32x32x16_bf16 v[4:19], v[28:31], v[40:43], v[4:19]
	s_waitcnt lgkmcnt(3)
	v_mfma_f32_32x32x16_bf16 v[4:19], v[32:35], v[44:47], v[4:19]
	s_waitcnt lgkmcnt(2)
	v_mfma_f32_32x32x16_bf16 v[4:19], v[82:85], v[48:51], v[4:19]
	s_waitcnt lgkmcnt(1)
	v_mfma_f32_32x32x16_bf16 v[4:19], v[86:89], v[60:63], v[4:19]
	s_waitcnt lgkmcnt(0)
	v_mfma_f32_32x32x16_bf16 v[4:19], v[90:93], v[64:67], v[4:19]
	v_add_u32_e32 v24, 0x2000, v98
	ds_read2_b64 v[20:23], v24 offset0:32 offset1:34
	ds_read2_b64 v[82:85], v24 offset0:36 offset1:38
	ds_read2_b64 v[86:89], v24 offset0:40 offset1:42
	ds_read2_b64 v[90:93], v24 offset0:44 offset1:46
	ds_read2_b64 v[98:101], v24 offset0:48 offset1:50
	ds_read2_b64 v[102:105], v24 offset0:52 offset1:54
	ds_read2_b64 v[106:109], v24 offset0:56 offset1:58
	ds_read2_b64 v[110:113], v24 offset0:60 offset1:62
	s_waitcnt lgkmcnt(7)
	v_mfma_f32_32x32x16_bf16 v[20:35], v[20:23], v[52:55], 0
	s_waitcnt lgkmcnt(6)
	v_mfma_f32_32x32x16_bf16 v[20:35], v[82:85], v[56:59], v[20:35]
	s_waitcnt lgkmcnt(5)
	v_mfma_f32_32x32x16_bf16 v[20:35], v[86:89], v[36:39], v[20:35]
	s_waitcnt lgkmcnt(4)
	v_mfma_f32_32x32x16_bf16 v[20:35], v[90:93], v[40:43], v[20:35]
	s_waitcnt lgkmcnt(3)
	v_mfma_f32_32x32x16_bf16 v[20:35], v[98:101], v[44:47], v[20:35]
	s_waitcnt lgkmcnt(2)
	v_mfma_f32_32x32x16_bf16 v[20:35], v[102:105], v[48:51], v[20:35]
	s_waitcnt lgkmcnt(1)
	v_mfma_f32_32x32x16_bf16 v[20:35], v[106:109], v[60:63], v[20:35]
	s_waitcnt lgkmcnt(0)
	v_mfma_f32_32x32x16_bf16 v[20:35], v[110:113], v[64:67], v[20:35]
	v_add3_u32 v52, s33, v149, v153
	v_add_u32_e32 v64, 0x1000, v52
	ds_read2_b64 v[36:39], v52 offset1:2
	ds_read2_b64 v[40:43], v52 offset0:4 offset1:6
	ds_read2_b64 v[44:47], v52 offset0:8 offset1:10
	ds_read2_b64 v[48:51], v52 offset0:12 offset1:14
	ds_read2_b64 v[52:55], v64 offset0:32 offset1:34
	ds_read2_b64 v[56:59], v64 offset0:36 offset1:38
	ds_read2_b64 v[60:63], v64 offset0:40 offset1:42
	ds_read2_b64 v[64:67], v64 offset0:44 offset1:46
	s_waitcnt lgkmcnt(7)
	v_mfma_f32_32x32x16_bf16 v[4:19], v[36:39], v[68:71], v[4:19]
	s_waitcnt lgkmcnt(3)
	v_mfma_f32_32x32x16_bf16 v[20:35], v[52:55], v[68:71], v[20:35]
	v_mfma_f32_32x32x16_bf16 v[4:19], v[40:43], v[72:75], v[4:19]
	s_waitcnt lgkmcnt(2)
	v_mfma_f32_32x32x16_bf16 v[20:35], v[56:59], v[72:75], v[20:35]
	v_mfma_f32_32x32x16_bf16 v[4:19], v[44:47], v[78:81], v[4:19]
	s_waitcnt lgkmcnt(1)
	v_mfma_f32_32x32x16_bf16 v[20:35], v[60:63], v[78:81], v[20:35]
	v_mfma_f32_32x32x16_bf16 v[4:19], v[48:51], v[94:97], v[4:19]
	s_waitcnt lgkmcnt(0)
	v_mfma_f32_32x32x16_bf16 v[20:35], v[64:67], v[94:97], v[20:35]
	v_lshl_add_u64 v[36:37], v[76:77], 0, v[2:3]
	s_mov_b32 s9, 0x479e0000
	v_add_co_u32_e32 v38, vcc, s9, v36
	s_mov_b32 s9, 0x479e1000
	s_nop 0
	v_addc_co_u32_e32 v39, vcc, 0, v37, vcc
	s_nop 3
	global_store_dword v[38:39], v4, off
	global_store_dword v[38:39], v5, off offset:2048
	v_add_co_u32_e32 v4, vcc, s9, v36
	s_mov_b32 s9, 0x479e4000
	s_nop 0
	v_addc_co_u32_e32 v5, vcc, 0, v37, vcc
	global_store_dword v[4:5], v6, off
	global_store_dword v[4:5], v7, off offset:2048
	v_add_co_u32_e32 v4, vcc, s9, v36
	s_mov_b32 s9, 0x479e5000
	s_nop 0
	v_addc_co_u32_e32 v5, vcc, 0, v37, vcc
	global_store_dword v[4:5], v8, off
	global_store_dword v[4:5], v9, off offset:2048
	v_add_co_u32_e32 v4, vcc, s9, v36
	s_mov_b32 s9, 0x479e8000
	s_nop 0
	v_addc_co_u32_e32 v5, vcc, 0, v37, vcc
	global_store_dword v[4:5], v10, off
	global_store_dword v[4:5], v11, off offset:2048
	v_add_co_u32_e32 v4, vcc, s9, v36
	s_mov_b32 s9, 0x479e9000
	s_nop 0
	v_addc_co_u32_e32 v5, vcc, 0, v37, vcc
	global_store_dword v[4:5], v12, off
	global_store_dword v[4:5], v13, off offset:2048
	v_add_co_u32_e32 v4, vcc, s9, v36
	s_mov_b32 s9, 0x479ec000
	s_nop 0
	v_addc_co_u32_e32 v5, vcc, 0, v37, vcc
	global_store_dword v[4:5], v14, off
	global_store_dword v[4:5], v15, off offset:2048
	v_add_co_u32_e32 v4, vcc, s9, v36
	s_mov_b32 s9, 0x479ed000
	s_nop 0
	v_addc_co_u32_e32 v5, vcc, 0, v37, vcc
	global_store_dword v[4:5], v16, off
	global_store_dword v[4:5], v17, off offset:2048
	v_add_co_u32_e32 v4, vcc, s9, v36
	s_mov_b32 s9, 0x479f0000
	s_nop 0
	v_addc_co_u32_e32 v5, vcc, 0, v37, vcc
	global_store_dword v[4:5], v18, off
	global_store_dword v[4:5], v19, off offset:2048
	v_add_co_u32_e32 v4, vcc, s9, v36
	s_mov_b32 s9, 0x479f1000
	s_nop 0
	v_addc_co_u32_e32 v5, vcc, 0, v37, vcc
	global_store_dword v[4:5], v20, off
	global_store_dword v[4:5], v21, off offset:2048
	v_add_co_u32_e32 v4, vcc, s9, v36
	s_mov_b32 s9, 0x479f4000
	s_nop 0
	v_addc_co_u32_e32 v5, vcc, 0, v37, vcc
	global_store_dword v[4:5], v22, off
	global_store_dword v[4:5], v23, off offset:2048
	v_add_co_u32_e32 v4, vcc, s9, v36
	s_mov_b32 s9, 0x479f5000
	s_nop 0
	v_addc_co_u32_e32 v5, vcc, 0, v37, vcc
	global_store_dword v[4:5], v24, off
	global_store_dword v[4:5], v25, off offset:2048
	v_add_co_u32_e32 v4, vcc, s9, v36
	s_mov_b32 s9, 0x479f8000
	s_nop 0
	v_addc_co_u32_e32 v5, vcc, 0, v37, vcc
	global_store_dword v[4:5], v26, off
	global_store_dword v[4:5], v27, off offset:2048
	v_add_co_u32_e32 v4, vcc, s9, v36
	s_mov_b32 s9, 0x479f9000
	s_nop 0
	v_addc_co_u32_e32 v5, vcc, 0, v37, vcc
	global_store_dword v[4:5], v28, off
	global_store_dword v[4:5], v29, off offset:2048
	v_add_co_u32_e32 v4, vcc, s9, v36
	s_mov_b32 s9, 0x479fc000
	s_nop 0
	v_addc_co_u32_e32 v5, vcc, 0, v37, vcc
	global_store_dword v[4:5], v30, off
	global_store_dword v[4:5], v31, off offset:2048
	v_add_co_u32_e32 v4, vcc, s9, v36
	s_nop 1
	v_addc_co_u32_e32 v5, vcc, 0, v37, vcc
	global_store_dword v[4:5], v32, off
	global_store_dword v[4:5], v33, off offset:2048
	v_add_co_u32_e32 v4, vcc, 0x479fd000, v36
	s_nop 1
	v_addc_co_u32_e32 v5, vcc, 0, v37, vcc
	global_store_dword v[4:5], v34, off
	global_store_dword v[4:5], v35, off offset:2048
	s_mov_b64 s[28:29], 0
	s_waitcnt lgkmcnt(0)
	s_barrier
